# P2 work rebalanced (quad WGs take 2 LRU units, others 7) + write-through final out stores + strided expert counters
# speedup vs baseline: 1.0288x; 1.0058x over previous
; __device__ __forceinline__ void phase3(const Args& a, unsigned char* lds_g, int tid) {
;     {
;         int q0 = (int)blockIdx.x, qstep = (int)gridDim.x;
;         if (gridDim.x == 256) q0 = blockIdx.x >= 128 ? (int)blockIdx.x - 128 : 128;
;         for (int qu = q0; qu < 128; qu += qstep) ml_state_quad(a, lds_g, qu, tid);
;     }
;     bf16x8_t wl[2][2][4]; int wl_blk = -1;
;     for (int u = blockIdx.x; u < 4 * 36 * 8; u += gridDim.x) { const int blk = u & 7, q = u >> 3; lru_unit<false>(a, lds_g, q / 36, q % 36, blk, tid, wl, wl_blk); }
; }
.LBB0_282:
	s_cmpk_gt_i32 s83, 0x47f
	s_cbranch_scc1 .LBB0_315
	s_add_u32 s14, s84, 0x21000000
	s_addc_u32 s15, s85, 0
	s_add_u32 s48, s84, 0x500000
	s_addc_u32 s49, s85, 0
	s_add_u32 s2, s84, 0x3d200000
	s_addc_u32 s3, s85, 0
	v_mbcnt_lo_u32_b32 v0, -1, 0
	s_add_u32 s47, s84, 0x4800000
	v_mbcnt_hi_u32_b32 v185, -1, v0
	v_mov_b32_e32 v0, 0x80
	s_addc_u32 s64, s85, 0
	s_mov_b32 s42, -1
	v_mov_b32_e32 v129, 0
	s_movk_i32 s65, 0x1000
	s_movk_i32 s68, 0x100
	s_mov_b64 s[50:51], 0x1000
	s_mov_b64 s[54:55], 0x2000
	s_movk_i32 s69, 0x2000
	s_mov_b64 s[56:57], 0x3000
	s_movk_i32 s72, 0x3000
	s_movk_i32 s33, 0x210
	s_movk_i32 s34, 0x110
	s_mov_b32 s35, 0xc1a00000
	s_mov_b32 s36, 0x3f2aaaab
	v_mov_b32_e32 v181, 0x3ecc95a3
	s_mov_b32 s37, 0x3f317218
	s_mov_b32 s38, 0x7f800000
	s_mov_b32 s39, 0x33800000
	s_movk_i32 s40, 0x840
	v_mov_b32_e32 v130, 0x3f317218
	v_mov_b32_e32 v182, 0x7f800000
	v_mov_b32_e32 v183, 0x7fc00000
	v_mov_b32_e32 v184, 0xff800000
	v_mov_b32_e32 v186, 0xc0
	v_lshl_or_b32 v187, v185, 2, v0
	s_mov_b32 s101, s82
	s_movk_i32 s100, 0x480
	s_mov_b32 s41, s83
	s_cmpk_lg_i32 s82, 0x100
	s_cbranch_scc1 .Lp2_plain
	s_movk_i32 s101, 0x80
	s_add_i32 s41, s83, 0x300
	s_cmpk_lt_i32 s83, 0x80
	s_cselect_b32 s41, s83, s41
	s_cselect_b32 s100, 0x380, s100
.Lp2_plain:
	s_branch .LBB0_285
.LBB0_284:
	s_or_b64 exec, exec, s[6:7]
	s_waitcnt lgkmcnt(0)
	s_barrier
	s_add_i32 s41, s41, s101
	s_cmp_lt_i32 s41, s100
	s_cbranch_scc0 .LBB0_315

; __device__ __forceinline__ void phase12(const Args& a, unsigned char* lds_g, int lane, int wave) {
;     ...
;       for (int t = t0; t < t0 + 4; ++t) {
;         const int4 q0 = ASG[2 * t], q1 = ASG[2 * t + 1];
;         const float w0 = __int_as_float(q0.z), w1 = __int_as_float(q1.z);
;         const unsigned long long* xr = (const unsigned long long*)(X1 + (size_t)t * D) + lane;
;         const unsigned* y0 = (const unsigned*)(Y2 + (size_t)(256 * cum[q0.x] + q0.y) * D) + lane; const unsigned* y1 = (const unsigned*)(Y2 + (size_t)(256 * cum[q1.x] + q1.y) * D) + lane;
;         f32x4 v[8]; float s = 0.f;
; #pragma unroll
;         for (int j = 0; j < 8; ++j) {
;             const int c = 4 * lane + 256 * j;
;             const f32x4 g2 = g2v[j]; (void)c;
;             const unsigned a0 = y0[64 * j], a1 = y1[64 * j];
;             const auto l0 = __builtin_amdgcn_cvt_pk_f32_fp8((int)a0, false), h0 = __builtin_amdgcn_cvt_pk_f32_fp8((int)a0, true), l1 = __builtin_amdgcn_cvt_pk_f32_fp8((int)a1, false), h1 = __builtin_amdgcn_cvt_pk_f32_fp8((int)a1, true);
;             f32x4 y; y.x = w0 * l0[0] + w1 * l1[0]; y.y = w0 * l0[1] + w1 * l1[1]; y.z = w0 * h0[0] + w1 * h1[0]; y.w = w0 * h0[1] + w1 * h1[1];
;             const unsigned long long xw = xr[64 * j];
;             v[j] = (f32x4){bflo((unsigned)xw), bfhi((unsigned)xw), bflo((unsigned)(xw >> 32)), bfhi((unsigned)(xw >> 32))} + g2 * y;
.LBB0_1279:
	s_ashr_i32 s21, s20, 31
	s_lshl_b64 s[0:1], s[20:21], 4
	s_add_u32 s0, s24, s0
	s_addc_u32 s1, s25, s1
	global_load_dwordx2 v[86:87], v[82:83], off offset:-2048
	global_load_dwordx2 v[88:89], v[82:83], off offset:-1536
	global_load_dwordx2 v[90:91], v[82:83], off offset:-1024
	global_load_dwordx2 v[92:93], v[82:83], off offset:-512
	global_load_dwordx2 v[94:95], v[82:83], off
	global_load_dwordx2 v[96:97], v[82:83], off offset:512
	global_load_dwordx2 v[116:117], v[82:83], off offset:1024
	global_load_dwordx2 v[118:119], v[82:83], off offset:1536
	global_load_dwordx3 v[108:110], v65, s[0:1]
	global_load_dwordx3 v[112:114], v65, s[0:1] offset:16
	s_add_i32 s30, s30, 1
	s_add_i32 s20, s20, 2
	v_lshl_add_u64 v[82:83], v[82:83], 0, s[12:13]
	s_cmp_ge_i32 s30, s29
	s_waitcnt vmcnt(9)
	v_lshlrev_b32_e32 v120, 16, v86
	v_and_b32_e32 v121, 0xffff0000, v86
	v_lshlrev_b32_e32 v86, 16, v87
	v_and_b32_e32 v87, 0xffff0000, v87
	s_waitcnt vmcnt(8)
	v_lshlrev_b32_e32 v122, 16, v88
	v_and_b32_e32 v123, 0xffff0000, v88
	s_waitcnt vmcnt(1)
	v_lshlrev_b32_e32 v107, 2, v108
	s_waitcnt vmcnt(0)
	v_lshlrev_b32_e32 v111, 2, v112
	v_add_u32_e32 v107, s9, v107
	v_add_u32_e32 v111, s9, v111
	ds_read_b32 v107, v107
	ds_read_b32 v111, v111
	v_mov_b32_e32 v108, v114
	v_lshlrev_b32_e32 v88, 16, v89
	v_and_b32_e32 v89, 0xffff0000, v89
	s_waitcnt lgkmcnt(1)
	v_lshlrev_b32_e32 v107, 8, v107
	s_waitcnt lgkmcnt(0)
	v_lshlrev_b32_e32 v111, 8, v111
	v_add_u32_e32 v112, v107, v109
	v_add_u32_e32 v114, v111, v113
	v_ashrrev_i32_e32 v113, 31, v112
	v_ashrrev_i32_e32 v115, 31, v114
	v_lshlrev_b64 v[112:113], 11, v[112:113]
	v_lshlrev_b64 v[114:115], 11, v[114:115]
	v_lshl_add_u64 v[112:113], v[68:69], 0, v[112:113]
	v_lshl_add_u64 v[114:115], v[68:69], 0, v[114:115]
	global_load_dword v107, v[112:113], off
	global_load_dword v109, v[114:115], off
	global_load_dword v111, v[112:113], off offset:256
	global_load_dword v146, v[114:115], off offset:256
	global_load_dword v150, v[112:113], off offset:512
	global_load_dword v154, v[114:115], off offset:512
	global_load_dword v158, v[112:113], off offset:768
	global_load_dword v162, v[114:115], off offset:768
	global_load_dword v166, v[112:113], off offset:1024
	global_load_dword v170, v[114:115], off offset:1024
	global_load_dword v174, v[112:113], off offset:1280
	global_load_dword v178, v[114:115], off offset:1280
	global_load_dword v182, v[112:113], off offset:1536
	global_load_dword v186, v[114:115], off offset:1536
	global_load_dword v190, v[112:113], off offset:1792
	global_load_dword v194, v[114:115], off offset:1792
	v_lshlrev_b32_e32 v124, 16, v90
	v_and_b32_e32 v125, 0xffff0000, v90
	v_lshlrev_b32_e32 v90, 16, v91
	v_and_b32_e32 v91, 0xffff0000, v91
	v_lshlrev_b32_e32 v126, 16, v92
	v_and_b32_e32 v127, 0xffff0000, v92
	v_lshlrev_b32_e32 v130, 16, v96
	v_and_b32_e32 v131, 0xffff0000, v96
	v_lshlrev_b32_e32 v134, 16, v118
	v_and_b32_e32 v135, 0xffff0000, v118
	v_lshlrev_b32_e32 v128, 16, v94
	v_and_b32_e32 v129, 0xffff0000, v94
	v_lshlrev_b32_e32 v132, 16, v116
	v_and_b32_e32 v133, 0xffff0000, v116
	v_lshlrev_b32_e32 v118, 16, v119
	v_and_b32_e32 v119, 0xffff0000, v119
	v_lshlrev_b32_e32 v92, 16, v93
	v_and_b32_e32 v93, 0xffff0000, v93
	v_lshlrev_b32_e32 v96, 16, v97
	v_and_b32_e32 v97, 0xffff0000, v97
	v_lshlrev_b32_e32 v94, 16, v95
	v_and_b32_e32 v95, 0xffff0000, v95
	v_lshlrev_b32_e32 v116, 16, v117
	v_and_b32_e32 v117, 0xffff0000, v117
	s_waitcnt vmcnt(15)
	v_cvt_pk_f32_fp8_e32 v[112:113], v107
	s_waitcnt vmcnt(14)
	v_cvt_pk_f32_fp8_e32 v[136:137], v109
	v_cvt_pk_f32_fp8_sdwa v[138:139], v109 src0_sel:WORD_1
	s_waitcnt vmcnt(12)
	v_cvt_pk_f32_fp8_e32 v[144:145], v146
	v_cvt_pk_f32_fp8_sdwa v[146:147], v146 src0_sel:WORD_1
	v_cvt_pk_f32_fp8_sdwa v[114:115], v107 src0_sel:WORD_1
	v_cvt_pk_f32_fp8_e32 v[140:141], v111
	v_cvt_pk_f32_fp8_sdwa v[142:143], v111 src0_sel:WORD_1
	s_waitcnt vmcnt(10)
	v_cvt_pk_f32_fp8_e32 v[152:153], v154
	v_cvt_pk_f32_fp8_sdwa v[154:155], v154 src0_sel:WORD_1
	s_waitcnt vmcnt(8)
	v_cvt_pk_f32_fp8_e32 v[160:161], v162
	v_cvt_pk_f32_fp8_sdwa v[162:163], v162 src0_sel:WORD_1
	s_waitcnt vmcnt(6)
	v_cvt_pk_f32_fp8_e32 v[168:169], v170
	v_cvt_pk_f32_fp8_sdwa v[170:171], v170 src0_sel:WORD_1
	s_waitcnt vmcnt(4)
	v_cvt_pk_f32_fp8_e32 v[176:177], v178
	v_cvt_pk_f32_fp8_sdwa v[178:179], v178 src0_sel:WORD_1
	s_waitcnt vmcnt(2)
	v_cvt_pk_f32_fp8_e32 v[184:185], v186
	v_cvt_pk_f32_fp8_sdwa v[186:187], v186 src0_sel:WORD_1
	s_waitcnt vmcnt(0)
; __device__ __forceinline__ void phase12(const Args& a, unsigned char* lds_g, int lane, int wave) {
;     ...
;         for (int j = 0; j < 8; ++j) {
;             const int c = 4 * lane + 256 * j;
;             const f32x4 g2 = g2v[j]; (void)c;
;             const unsigned a0 = y0[64 * j], a1 = y1[64 * j];
;             const auto l0 = __builtin_amdgcn_cvt_pk_f32_fp8((int)a0, false), h0 = __builtin_amdgcn_cvt_pk_f32_fp8((int)a0, true), l1 = __builtin_amdgcn_cvt_pk_f32_fp8((int)a1, false), h1 = __builtin_amdgcn_cvt_pk_f32_fp8((int)a1, true);
;             f32x4 y; y.x = w0 * l0[0] + w1 * l1[0]; y.y = w0 * l0[1] + w1 * l1[1]; y.z = w0 * h0[0] + w1 * h1[0]; y.w = w0 * h0[1] + w1 * h1[1];
;             const unsigned long long xw = xr[64 * j];
;             v[j] = (f32x4){bflo((unsigned)xw), bfhi((unsigned)xw), bflo((unsigned)(xw >> 32)), bfhi((unsigned)(xw >> 32))} + g2 * y;
;             s += (v[j].x * v[j].x + v[j].y * v[j].y) + (v[j].z * v[j].z + v[j].w * v[j].w);
;         }
	v_cvt_pk_f32_fp8_e32 v[192:193], v194
	v_cvt_pk_f32_fp8_sdwa v[194:195], v194 src0_sel:WORD_1
	v_cvt_pk_f32_fp8_e32 v[148:149], v150
	v_cvt_pk_f32_fp8_sdwa v[150:151], v150 src0_sel:WORD_1
	v_cvt_pk_f32_fp8_e32 v[156:157], v158
	v_cvt_pk_f32_fp8_e32 v[172:173], v174
	v_cvt_pk_f32_fp8_e32 v[188:189], v190
	v_cvt_pk_f32_fp8_sdwa v[158:159], v158 src0_sel:WORD_1
	v_cvt_pk_f32_fp8_e32 v[164:165], v166
	v_cvt_pk_f32_fp8_sdwa v[166:167], v166 src0_sel:WORD_1
	v_cvt_pk_f32_fp8_sdwa v[174:175], v174 src0_sel:WORD_1
	v_cvt_pk_f32_fp8_e32 v[180:181], v182
	v_cvt_pk_f32_fp8_sdwa v[182:183], v182 src0_sel:WORD_1
	v_cvt_pk_f32_fp8_sdwa v[190:191], v190 src0_sel:WORD_1
	v_pk_mul_f32 v[138:139], v[108:109], v[138:139] op_sel_hi:[0,1]
	v_pk_mul_f32 v[136:137], v[108:109], v[136:137] op_sel_hi:[0,1]
	v_pk_mul_f32 v[146:147], v[108:109], v[146:147] op_sel_hi:[0,1]
	v_pk_mul_f32 v[144:145], v[108:109], v[144:145] op_sel_hi:[0,1]
	v_pk_mul_f32 v[152:153], v[108:109], v[152:153] op_sel_hi:[0,1]
	v_pk_mul_f32 v[154:155], v[108:109], v[154:155] op_sel_hi:[0,1]
	v_pk_mul_f32 v[162:163], v[108:109], v[162:163] op_sel_hi:[0,1]
	v_pk_mul_f32 v[160:161], v[108:109], v[160:161] op_sel_hi:[0,1]
	v_pk_mul_f32 v[170:171], v[108:109], v[170:171] op_sel_hi:[0,1]
	v_pk_mul_f32 v[168:169], v[108:109], v[168:169] op_sel_hi:[0,1]
	v_pk_mul_f32 v[176:177], v[108:109], v[176:177] op_sel_hi:[0,1]
	v_pk_mul_f32 v[178:179], v[108:109], v[178:179] op_sel_hi:[0,1]
	v_pk_mul_f32 v[186:187], v[108:109], v[186:187] op_sel_hi:[0,1]
	v_pk_mul_f32 v[184:185], v[108:109], v[184:185] op_sel_hi:[0,1]
	v_pk_mul_f32 v[194:195], v[108:109], v[194:195] op_sel_hi:[0,1]
	v_pk_mul_f32 v[108:109], v[108:109], v[192:193] op_sel_hi:[0,1]
	v_pk_fma_f32 v[112:113], v[110:111], v[112:113], v[136:137] op_sel_hi:[0,1,1]
	v_pk_fma_f32 v[114:115], v[110:111], v[114:115], v[138:139] op_sel_hi:[0,1,1]
	v_pk_fma_f32 v[136:137], v[110:111], v[140:141], v[144:145] op_sel_hi:[0,1,1]
	v_pk_fma_f32 v[138:139], v[110:111], v[142:143], v[146:147] op_sel_hi:[0,1,1]
	v_pk_fma_f32 v[140:141], v[110:111], v[150:151], v[154:155] op_sel_hi:[0,1,1]
	v_pk_fma_f32 v[142:143], v[110:111], v[148:149], v[152:153] op_sel_hi:[0,1,1]
	v_pk_fma_f32 v[144:145], v[110:111], v[156:157], v[160:161] op_sel_hi:[0,1,1]
	v_pk_fma_f32 v[154:155], v[110:111], v[172:173], v[176:177] op_sel_hi:[0,1,1]
	v_pk_fma_f32 v[108:109], v[110:111], v[188:189], v[108:109] op_sel_hi:[0,1,1]
	v_pk_fma_f32 v[86:87], v[10:11], v[114:115], v[86:87]
	v_pk_fma_f32 v[112:113], v[8:9], v[112:113], v[120:121]
	v_pk_fma_f32 v[88:89], v[14:15], v[138:139], v[88:89]
	v_pk_fma_f32 v[114:115], v[12:13], v[136:137], v[122:123]
	v_pk_fma_f32 v[146:147], v[110:111], v[158:159], v[162:163] op_sel_hi:[0,1,1]
	v_pk_fma_f32 v[148:149], v[110:111], v[164:165], v[168:169] op_sel_hi:[0,1,1]
	v_pk_fma_f32 v[150:151], v[110:111], v[166:167], v[170:171] op_sel_hi:[0,1,1]
	v_pk_fma_f32 v[152:153], v[110:111], v[174:175], v[178:179] op_sel_hi:[0,1,1]
	v_pk_fma_f32 v[156:157], v[110:111], v[180:181], v[184:185] op_sel_hi:[0,1,1]
	v_pk_fma_f32 v[158:159], v[110:111], v[182:183], v[186:187] op_sel_hi:[0,1,1]
	v_pk_fma_f32 v[110:111], v[110:111], v[190:191], v[194:195] op_sel_hi:[0,1,1]
	v_pk_fma_f32 v[120:121], v[20:21], v[142:143], v[124:125]
	v_pk_fma_f32 v[90:91], v[22:23], v[140:141], v[90:91]
	v_pk_fma_f32 v[122:123], v[28:29], v[144:145], v[126:127]
	v_pk_fma_f32 v[126:127], v[44:45], v[154:155], v[130:131]
	v_pk_fma_f32 v[108:109], v[60:61], v[108:109], v[134:135]
	v_mov_b32_e32 v130, v113
	v_mov_b32_e32 v131, v115
	v_mov_b32_e32 v134, v87
	v_mov_b32_e32 v135, v89
	v_pk_fma_f32 v[124:125], v[36:37], v[148:149], v[128:129]
	v_pk_fma_f32 v[128:129], v[52:53], v[156:157], v[132:133]
	v_pk_fma_f32 v[110:111], v[62:63], v[110:111], v[118:119]
	v_mov_b32_e32 v118, v112
	v_mov_b32_e32 v119, v114
	v_mov_b32_e32 v132, v86
	v_mov_b32_e32 v133, v88
	v_pk_mul_f32 v[136:137], v[90:91], v[90:91]
	v_pk_mul_f32 v[138:139], v[120:121], v[120:121]
	v_pk_mul_f32 v[130:131], v[130:131], v[130:131]
	v_pk_mul_f32 v[134:135], v[134:135], v[134:135]
	v_pk_fma_f32 v[92:93], v[30:31], v[146:147], v[92:93]
	v_pk_fma_f32 v[96:97], v[46:47], v[152:153], v[96:97]
	v_pk_mov_b32 v[152:153], v[138:139], v[136:137] op_sel:[1,0]
	v_mov_b32_e32 v139, v137
	v_pk_fma_f32 v[118:119], v[118:119], v[118:119], v[130:131]
	v_pk_fma_f32 v[130:131], v[132:133], v[132:133], v[134:135]
	v_pk_fma_f32 v[94:95], v[38:39], v[150:151], v[94:95]
	v_mul_f32_e32 v140, v123, v123
	v_mul_f32_e32 v142, v93, v93
	v_pk_add_f32 v[132:133], v[152:153], v[138:139]
	v_pk_add_f32 v[118:119], v[118:119], v[130:131]
	v_mul_f32_e32 v107, v124, v124
	v_mul_f32_e32 v151, v125, v125
	v_mul_f32_e32 v154, v94, v94
	v_mul_f32_e32 v155, v95, v95
	v_pk_fma_f32 v[136:137], v[122:123], v[122:123], v[140:141] op_sel_hi:[1,1,0]
	v_pk_fma_f32 v[140:141], v[92:93], v[92:93], v[142:143] op_sel_hi:[1,1,0]
	v_pk_add_f32 v[130:131], v[132:133], v[132:133] op_sel:[0,1] op_sel_hi:[1,0]
	v_pk_add_f32 v[118:119], v[118:119], v[118:119] op_sel:[0,1] op_sel_hi:[1,0]
	v_pk_mul_f32 v[144:145], v[96:97], v[96:97]
	v_pk_mul_f32 v[146:147], v[126:127], v[126:127]
	v_mov_b32_e32 v137, v154
	v_mov_b32_e32 v141, v155
	v_mov_b32_e32 v131, v151
	v_mov_b32_e32 v119, v107
	v_pk_fma_f32 v[116:117], v[54:55], v[158:159], v[116:117]
	v_pk_mov_b32 v[142:143], v[146:147], v[144:145] op_sel:[1,0]
	v_mov_b32_e32 v147, v145
	v_pk_add_f32 v[132:133], v[136:137], v[140:141]
	v_pk_add_f32 v[118:119], v[118:119], v[130:131]
	v_mul_f32_e32 v148, v129, v129
	v_mul_f32_e32 v150, v117, v117
	v_pk_add_f32 v[134:135], v[142:143], v[146:147]
	v_pk_add_f32 v[118:119], v[118:119], v[132:133]
	v_mul_f32_e32 v156, v108, v108
	v_mul_f32_e32 v157, v109, v109
	v_mul_f32_e32 v158, v110, v110
	v_mul_f32_e32 v159, v111, v111
	v_pk_fma_f32 v[144:145], v[128:129], v[128:129], v[148:149] op_sel_hi:[1,1,0]
	v_pk_fma_f32 v[148:149], v[116:117], v[116:117], v[150:151] op_sel_hi:[1,1,0]
	v_pk_add_f32 v[134:135], v[134:135], v[134:135] op_sel:[0,1] op_sel_hi:[1,0]
	v_pk_add_f32 v[118:119], v[118:119], v[118:119] op_sel:[0,1] op_sel_hi:[1,0]
	v_mov_b32_e32 v145, v158
	v_mov_b32_e32 v149, v159
	v_mov_b32_e32 v135, v157
	v_mov_b32_e32 v119, v156
	v_pk_add_f32 v[136:137], v[144:145], v[148:149]
	v_pk_add_f32 v[118:119], v[118:119], v[134:135]
	s_nop 0
	v_pk_add_f32 v[118:119], v[118:119], v[136:137]
	s_nop 0
	v_add_f32_e32 v107, v118, v119
	ds_bpermute_b32 v118, v99, v107
	s_waitcnt lgkmcnt(0)
; __device__ __forceinline__ float wave_sum(float v) {
; #pragma unroll
;     for (int o = 1; o < 64; o <<= 1) v += __shfl_xor(v, o);
;     return v;
; __device__ __forceinline__ void phase12(const Args& a, unsigned char* lds_g, int lane, int wave) {
;     ...
;         const float rstd = 1.f / sqrtf(wave_sum(s) * (1.f / D) + EPS);
;         f32x4* o = (f32x4*)(a.out + (size_t)t * D) + lane;
; #pragma unroll
;         for (int j = 0; j < 8; ++j) o[64 * j] = v[j] * rstd * fgv[j];
	v_add_f32_e32 v107, v107, v118
	ds_bpermute_b32 v118, v100, v107
	s_waitcnt lgkmcnt(0)
	v_add_f32_e32 v107, v107, v118
	ds_bpermute_b32 v118, v101, v107
	s_waitcnt lgkmcnt(0)
	v_add_f32_e32 v107, v107, v118
	ds_bpermute_b32 v118, v102, v107
	s_waitcnt lgkmcnt(0)
	v_add_f32_e32 v107, v107, v118
	ds_bpermute_b32 v118, v103, v107
	s_waitcnt lgkmcnt(0)
	v_add_f32_e32 v107, v107, v118
	ds_bpermute_b32 v118, v104, v107
	s_waitcnt lgkmcnt(0)
	v_add_f32_e32 v107, v107, v118
	v_fmamk_f32 v107, v107, 0x3a000000, v105
	v_mul_f32_e32 v118, 0x4f800000, v107
	v_cmp_gt_f32_e32 vcc, s11, v107
	s_nop 1
	v_cndmask_b32_e32 v107, v107, v118, vcc
	v_sqrt_f32_e32 v118, v107
	s_nop 0
	v_add_u32_e32 v119, -1, v118
	v_add_u32_e32 v130, 1, v118
	v_fma_f32 v131, -v119, v118, v107
	v_fma_f32 v132, -v130, v118, v107
	v_cmp_ge_f32_e64 s[0:1], 0, v131
	s_nop 1
	v_cndmask_b32_e64 v118, v118, v119, s[0:1]
	v_cmp_lt_f32_e64 s[0:1], 0, v132
	s_nop 1
	v_cndmask_b32_e64 v118, v118, v130, s[0:1]
	v_mul_f32_e32 v119, 0x37800000, v118
	v_cndmask_b32_e32 v118, v118, v119, vcc
	v_cmp_class_f32_e32 vcc, v107, v106
	s_nop 1
	v_cndmask_b32_e32 v107, v118, v107, vcc
	v_div_scale_f32 v118, s[0:1], v107, v107, 1.0
	v_rcp_f32_e32 v130, v118
	v_div_scale_f32 v119, vcc, 1.0, v107, 1.0
	v_fma_f32 v131, -v118, v130, 1.0
	v_fmac_f32_e32 v130, v131, v130
	v_mul_f32_e32 v131, v119, v130
	v_fma_f32 v132, -v118, v131, v119
	v_fmac_f32_e32 v131, v132, v130
	v_fma_f32 v118, -v118, v131, v119
	v_div_fmas_f32 v118, v118, v130, v131
	v_div_fixup_f32 v118, v118, v107, 1.0
	v_pk_mul_f32 v[112:113], v[112:113], v[118:119] op_sel_hi:[1,0]
	v_pk_mul_f32 v[86:87], v[86:87], v[118:119] op_sel_hi:[1,0]
	v_pk_mul_f32 v[114:115], v[114:115], v[118:119] op_sel_hi:[1,0]
	v_pk_mul_f32 v[130:131], v[88:89], v[118:119] op_sel_hi:[1,0]
	v_pk_mul_f32 v[120:121], v[120:121], v[118:119] op_sel_hi:[1,0]
	v_pk_mul_f32 v[132:133], v[90:91], v[118:119] op_sel_hi:[1,0]
	v_pk_mul_f32 v[122:123], v[122:123], v[118:119] op_sel_hi:[1,0]
	v_pk_mul_f32 v[134:135], v[92:93], v[118:119] op_sel_hi:[1,0]
	v_pk_mul_f32 v[124:125], v[124:125], v[118:119] op_sel_hi:[1,0]
	v_pk_mul_f32 v[136:137], v[94:95], v[118:119] op_sel_hi:[1,0]
	v_pk_mul_f32 v[126:127], v[126:127], v[118:119] op_sel_hi:[1,0]
	v_pk_mul_f32 v[138:139], v[96:97], v[118:119] op_sel_hi:[1,0]
	v_pk_mul_f32 v[128:129], v[128:129], v[118:119] op_sel_hi:[1,0]
	v_pk_mul_f32 v[140:141], v[116:117], v[118:119] op_sel_hi:[1,0]
	v_pk_mul_f32 v[142:143], v[108:109], v[118:119] op_sel_hi:[1,0]
	v_pk_mul_f32 v[144:145], v[110:111], v[118:119] op_sel_hi:[1,0]
	v_pk_mul_f32 v[88:89], v[2:3], v[86:87]
	v_pk_mul_f32 v[86:87], v[0:1], v[112:113]
	v_pk_mul_f32 v[92:93], v[6:7], v[130:131]
	v_pk_mul_f32 v[90:91], v[4:5], v[114:115]
	v_pk_mul_f32 v[96:97], v[18:19], v[132:133]
	v_pk_mul_f32 v[94:95], v[16:17], v[120:121]
	v_pk_mul_f32 v[110:111], v[26:27], v[134:135]
	v_pk_mul_f32 v[108:109], v[24:25], v[122:123]
	v_pk_mul_f32 v[114:115], v[34:35], v[136:137]
	v_pk_mul_f32 v[112:113], v[32:33], v[124:125]
	v_pk_mul_f32 v[118:119], v[42:43], v[138:139]
	v_pk_mul_f32 v[116:117], v[40:41], v[126:127]
	v_pk_mul_f32 v[122:123], v[50:51], v[140:141]
	v_pk_mul_f32 v[120:121], v[48:49], v[128:129]
	v_pk_mul_f32 v[126:127], v[58:59], v[144:145]
	v_pk_mul_f32 v[124:125], v[56:57], v[142:143]
	global_store_dwordx4 v[84:85], v[86:89], off offset:-4096 sc0 sc1
	global_store_dwordx4 v[84:85], v[90:93], off offset:-3072 sc0 sc1
	global_store_dwordx4 v[84:85], v[94:97], off offset:-2048 sc0 sc1
	global_store_dwordx4 v[84:85], v[108:111], off offset:-1024 sc0 sc1
	global_store_dwordx4 v[84:85], v[112:115], off sc0 sc1
	global_store_dwordx4 v[84:85], v[116:119], off offset:1024 sc0 sc1
	global_store_dwordx4 v[84:85], v[120:123], off offset:2048 sc0 sc1
	global_store_dwordx4 v[84:85], v[124:127], off offset:3072 sc0 sc1
	v_lshl_add_u64 v[84:85], v[84:85], 0, s[18:19]
	s_cbranch_scc0 .LBB0_1279
	s_add_i32 s8, s8, s10
	s_add_i32 s26, s26, s10
	s_add_i32 s27, s27, s28
	v_lshl_add_u64 v[78:79], v[78:79], 0, s[2:3]
	s_cmpk_gt_i32 s8, 0x1fff
	v_lshl_add_u64 v[80:81], v[80:81], 0, s[14:15]
	s_cbranch_scc0 .LBB0_1274
